# speedup vs baseline: 1.0328x; 1.0328x over previous
.LBB0_89:
	v_mov_b32_e32 v112, v22
	v_mov_b32_e32 v113, v23
	v_mov_b32_e32 v114, v24
	v_mov_b32_e32 v115, v25
	v_mov_b32_e32 v3, 0
	v_lshlrev_b32_e32 v70, 4, v28
	s_and_saveexec_b64 s[60:61], vcc
	s_cbranch_execz .LBB0_118
	s_mov_b64 s[92:93], s[14:15]
	v_lshl_add_u64 v[22:23], s[12:13], 0, v[2:3]
	s_waitcnt vmcnt(0) lgkmcnt(0)
	v_cndmask_b32_e64 v55, -1, v4, s[0:1]
	s_movk_i32 s0, 0x880
	v_mov_b32_e32 v2, 0x1dd00
	v_mad_u32_u24 v4, v80, s0, v2
	v_lshlrev_b32_e32 v2, 1, v1
	v_mov_b32_e32 v27, v3
	v_mbcnt_hi_u32_b32 v2, -1, v29
	v_lshl_add_u64 v[72:73], v[22:23], 0, v[26:27]
	v_and_b32_e32 v23, 64, v2
	v_xor_b32_e32 v22, 16, v2
	v_add_u32_e32 v23, 64, v23
	v_cmp_lt_i32_e32 vcc, v22, v23
	v_lshlrev_b32_e32 v88, 2, v28
	v_and_b32_e32 v24, 7, v0
	v_cndmask_b32_e32 v22, v2, v22, vcc
	v_lshlrev_b32_e32 v90, 2, v22
	v_xor_b32_e32 v22, 32, v2
	v_cmp_lt_i32_e32 vcc, v22, v23
	s_mov_b32 s24, 0x10000
	v_cndmask_b32_e32 v2, v2, v22, vcc
	v_lshlrev_b32_e32 v91, 2, v2
	v_lshrrev_b32_e32 v2, 2, v79
	v_mul_u32_u24_e32 v22, 0x88, v79
	v_add3_u32 v92, v4, v22, v1
	v_or_b32_e32 v2, v88, v2
	v_lshlrev_b32_e32 v22, 3, v0
	v_mul_u32_u24_e32 v2, 0x88, v2
	v_and_b32_e32 v22, 24, v22
	v_add3_u32 v93, v4, v2, v22
	v_lshrrev_b32_e32 v104, 1, v79
	v_and_b32_e32 v104, 3, v104
	v_lshrrev_b32_e32 v105, 3, v79
	v_and_b32_e32 v106, 1, v79
	v_lshl_add_u32 v105, v105, 1, v106
	v_add_u32_e32 v105, v105, v28
	v_and_b32_e32 v105, 3, v105
	v_lshlrev_b32_e32 v105, 3, v105
	v_lshl_add_u32 v105, v79, 7, v105
	v_add_u32_e32 v105, v105, v4
	v_lshl_add_u32 v92, v104, 5, v105
	v_add_u32_e32 v106, 1, v104
	v_and_b32_e32 v106, 3, v106
	v_lshl_add_u32 v116, v106, 5, v105
	v_add_u32_e32 v106, 2, v104
	v_and_b32_e32 v106, 3, v106
	v_lshl_add_u32 v117, v106, 5, v105
	v_add_u32_e32 v106, 3, v104
	v_and_b32_e32 v106, 3, v106
	v_lshl_add_u32 v118, v106, 5, v105
	v_lshrrev_b32_e32 v106, 2, v79
	v_lshl_add_u32 v106, v28, 2, v106
	v_lshrrev_b32_e32 v107, 1, v106
	v_and_b32_e32 v107, 3, v107
	v_lshrrev_b32_e32 v108, 3, v106
	v_and_b32_e32 v109, 1, v106
	v_lshl_add_u32 v108, v108, 1, v109
	v_and_b32_e32 v109, 3, v79
	v_add_u32_e32 v108, v108, v109
	v_and_b32_e32 v108, 3, v108
	v_lshlrev_b32_e32 v108, 3, v108
	v_lshl_add_u32 v108, v106, 7, v108
	v_add_u32_e32 v108, v108, v4
	v_lshl_add_u32 v93, v107, 5, v108
	v_add_u32_e32 v109, 1, v107
	v_and_b32_e32 v109, 3, v109
	v_lshl_add_u32 v119, v109, 5, v108
	v_add_u32_e32 v109, 2, v107
	v_and_b32_e32 v109, 3, v109
	v_lshl_add_u32 v110, v109, 5, v108
	v_add_u32_e32 v109, 3, v107
	v_and_b32_e32 v109, 3, v109
	v_lshl_add_u32 v111, v109, 5, v108
	v_lshlrev_b32_e32 v2, 5, v24
	v_or3_b32 v78, v2, v1, s24
	v_bfe_u32 v2, v0, 1, 2
	v_lshrrev_b32_e32 v89, 3, v79
	v_cmp_eq_u32_e64 s[6:7], 4, v24
	v_cmp_eq_u32_e64 s[8:9], 3, v24
	v_cmp_eq_u32_e64 s[10:11], 2, v24
	v_cmp_eq_u32_e64 s[12:13], 1, v24
	v_cmp_eq_u32_e64 s[14:15], 0, v24
	v_cmp_eq_u32_e64 s[16:17], 7, v24
	v_cmp_eq_u32_e64 s[18:19], 6, v24
	v_cmp_eq_u32_e64 s[20:21], 5, v24
	v_cmp_eq_u32_e64 s[22:23], 0, v2
	v_cmp_eq_u32_e64 s[24:25], 1, v2
	v_cmp_eq_u32_e64 s[26:27], 2, v2
	v_cmp_eq_u32_e64 s[28:29], 3, v2
	s_and_b64 s[22:23], s[22:23], s[4:5]
	s_and_b64 s[24:25], s[24:25], s[4:5]
	s_and_b64 s[26:27], s[26:27], s[4:5]
	s_and_b64 s[28:29], s[28:29], s[4:5]
	v_mov_b32_e32 v71, 0xf149f2ca
	s_mov_b64 s[62:63], 0
	s_mov_b32 s69, 0xf149f2ca
	s_mov_b32 s70, 0xefa18f08
	s_mov_b32 s71, 0x41000000
	s_movk_i32 s72, 0x110
	s_mov_b32 s77, 0x26500
	s_mov_b32 s73, 0x2650c
	s_mov_b32 s80, -1
	s_mov_b32 s81, 0
	s_mov_b32 s82, 0
	s_mov_b32 s83, 0x7fffffff
	s_mov_b64 s[84:85], 0
	v_mov_b32_e32 v100, 0
	v_mov_b32_e32 v4, 0
	v_mov_b32_e32 v103, 0xf149f2ca
	v_mov_b32_e32 v46, v3
	v_mov_b32_e32 v47, v3
	v_mov_b32_e32 v48, v3
	v_mov_b32_e32 v49, v3
	v_mov_b32_e32 v50, v3
	v_mov_b32_e32 v51, v3
	v_mov_b32_e32 v52, v3
	v_mov_b32_e32 v53, v3
	v_mov_b32_e32 v38, v3
	v_mov_b32_e32 v39, v3
	v_mov_b32_e32 v40, v3
	v_mov_b32_e32 v41, v3
	v_mov_b32_e32 v42, v3
	v_mov_b32_e32 v43, v3
	v_mov_b32_e32 v44, v3
	v_mov_b32_e32 v45, v3
	v_mov_b32_e32 v30, v3
	v_mov_b32_e32 v31, v3
	v_mov_b32_e32 v32, v3
	v_mov_b32_e32 v33, v3
	v_mov_b32_e32 v34, v3
	v_mov_b32_e32 v35, v3
	v_mov_b32_e32 v36, v3
	v_mov_b32_e32 v37, v3
	v_mov_b32_e32 v22, v3
	v_mov_b32_e32 v23, v3
	v_mov_b32_e32 v24, v3
	v_mov_b32_e32 v25, v3
	v_mov_b32_e32 v26, v3
	v_mov_b32_e32 v28, v3
	v_mov_b32_e32 v29, v3
	v_readfirstlane_b32 s86, v80
	s_mov_b32 s87, 0
	v_readfirstlane_b32 s88, v99
	v_readfirstlane_b32 s89, v5
	v_readfirstlane_b32 s96, v54
	v_readfirstlane_b32 s97, v84
	v_readfirstlane_b32 s98, v85
	v_readfirstlane_b32 s99, v81
	v_readfirstlane_b32 s100, v83
	v_readfirstlane_b32 s101, v82
	v_mov_b32_e32 v84, v82
	v_mov_b32_e32 v80, v116
	v_mov_b32_e32 v81, v117
	v_mov_b32_e32 v82, v118
	v_mov_b32_e32 v83, v119
	v_mov_b32_e32 v85, v110
	v_mov_b32_e32 v87, v111
	s_cmp_ge_i32 s96, s68
	s_cselect_b32 s100, 0, s100
	s_branch .LBB0_95

.LBB0_102:
	v_sub_f32_e32 v105, v105, v5
	v_sub_f32_e32 v104, v104, v5
	v_exp_f32_e32 v105, v105
	v_exp_f32_e32 v104, v104
	v_sub_f32_e32 v103, v107, v5
	ds_write_b64 v92, v[66:67]
	ds_write_b64 v80, v[68:69]
	ds_write_b64 v81, v[62:63]
	ds_write_b64 v82, v[64:65]
	ds_read_b64_tr_b16 v[62:63], v93
	ds_read_b64_tr_b16 v[64:65], v83
	v_cndmask_b32_e64 v107, v105, 0, s[40:41]
	v_cndmask_b32_e64 v108, v104, 0, s[44:45]
	ds_read_b64_tr_b16 v[68:69], v85
	ds_read_b64_tr_b16 v[104:105], v87
	ds_write_b64 v92, v[58:59]
	ds_write_b64 v80, v[60:61]
	ds_write_b64 v81, v[54:55]
	ds_write_b64 v82, v[56:57]
	ds_read_b64_tr_b16 v[54:55], v93
	v_sub_f32_e32 v106, v106, v5
	v_exp_f32_e32 v103, v103
	v_exp_f32_e32 v106, v106
	ds_read_b64_tr_b16 v[56:57], v83
	ds_read_b64_tr_b16 v[58:59], v85
	ds_read_b64_tr_b16 v[60:61], v87
	v_cndmask_b32_e64 v103, v103, 0, s[46:47]
	v_cndmask_b32_e64 v106, v106, 0, s[42:43]
	v_cvt_pk_f16_f32 v67, v106, v108
	v_cvt_pk_f16_f32 v66, v103, v107
	s_waitcnt lgkmcnt(3)
	s_cmp_eq_u32 s81, 0
	s_cbranch_scc1 .Lattn_g_first
	v_mfma_f32_16x16x16_f16 v[30:33], v[54:55], v[66:67], v[30:33]
	v_add_f32_e32 v54, 0, v103
	v_add_f32_e32 v54, v107, v54
	v_add_f32_e32 v54, v106, v54
	v_mfma_f32_16x16x16_f16 v[46:49], v[62:63], v[66:67], v[46:49]
	v_add_f32_e32 v54, v108, v54
	v_fmac_f32_e32 v54, v4, v2
	v_mfma_f32_16x16x16_f16 v[50:53], v[64:65], v[66:67], v[50:53]
	v_mfma_f32_16x16x16_f16 v[38:41], v[68:69], v[66:67], v[38:41]
	v_mfma_f32_16x16x16_f16 v[42:45], v[104:105], v[66:67], v[42:45]
	s_waitcnt lgkmcnt(2)
	v_mfma_f32_16x16x16_f16 v[34:37], v[56:57], v[66:67], v[34:37]
	s_waitcnt lgkmcnt(1)
	v_mfma_f32_16x16x16_f16 v[22:25], v[58:59], v[66:67], v[22:25]
	s_waitcnt lgkmcnt(0)
	v_mfma_f32_16x16x16_f16 v[26:29], v[60:61], v[66:67], v[26:29]
	s_branch .Lattn_g_done
